# MoE GEMM2: next unit's tile-completion counter requested one unit ahead; completed tiles skip the blocking poll and its queue drain
# baseline (speedup 1.0000x reference)
; #define LAS __attribute__((address_space(3)))
;     __device__ __forceinline__ void init(LAS unsigned char* lds, const bf16_t* A_, const int* ltok_, const bf16_t* Bt_, const int* cnt, int G, int c) {
;     ...
;         const int U = __builtin_amdgcn_readfirstlane(t[32]), xg = c & 7;
;         nw = (G + 7 - xg) >> 3; rk = REV_ ? nw - 1 - (c >> 3) : (c >> 3);
;         lo = (int)(((long)xg * U) >> 3); hi = (int)(((long)(xg + 1) * U) >> 3);
;         if (tidi < 16) { Unit u; const bool ok = next_slow<false>(tidi, u); LAS int* r = t + (ULIST_OFF - PRE_OFF) / 4 + tidi * 8;
;             r[0] = ok ? u.e : -1; r[1] = u.rt; r[2] = u.pn; r[3] = u.cnt; r[4] = u.rowbase; }
;         __syncthreads();
;     }
;     template <bool UNI>
;     __device__ __forceinline__ bool next_slow(int i, Unit& u) const {
;         const int g = lo + rk + i * nw; if (g >= hi) return false;
;         int e = 0;
; #pragma unroll
;         for (int st = 16; st > 0; st >>= 1) { const int v = UNI ? __builtin_amdgcn_readfirstlane(tb[e + st]) : tb[e + st]; if (v <= g) e += st; }
;         const int p = tb[e], cn = tb[66 + e], ro = tb[33 + e];
;         const int loc = g - (UNI ? __builtin_amdgcn_readfirstlane(p) : p);
;         u.e = e; u.rt = loc / NTN; u.pn = loc % NTN; u.cnt = UNI ? __builtin_amdgcn_readfirstlane(cn) : cn; u.rowbase = UNI ? __builtin_amdgcn_readfirstlane(ro) : ro;
.LBB0_1388:
	s_or_b64 exec, exec, s[2:3]
	v_mov_b32_e32 v255, 0
	s_add_i32 s2, s61, 0x20880
	v_mov_b32_e32 v2, s2
	s_waitcnt lgkmcnt(0)
	s_barrier
	ds_read_b32 v2, v2
	s_and_b32 s8, s11, 7
	s_sub_i32 s2, s10, s8
	s_add_i32 s2, s2, 7
	s_ashr_i32 s31, s2, 3
	s_ashr_i32 s2, s11, 3
	s_waitcnt lgkmcnt(0)
	v_readfirstlane_b32 s9, v2
	s_not_b32 s2, s2
	s_add_i32 s60, s31, s2
	s_mul_hi_i32 s3, s9, s8
	s_mul_i32 s2, s9, s8
	s_add_i32 s8, s8, 1
	s_lshr_b64 s[14:15], s[2:3], 3
	s_mul_hi_i32 s3, s9, s8
	s_mul_i32 s2, s9, s8
	s_lshr_b64 s[8:9], s[2:3], 3
	v_cmp_gt_i32_e32 vcc, 16, v20
	s_and_saveexec_b64 s[2:3], vcc
	s_cbranch_execz .LBB0_1392
	v_mul_lo_u32 v2, v20, s31
	s_add_i32 s9, s14, s60
	v_add_u32_e32 v4, s9, v2
	v_cmp_gt_i32_e32 vcc, s8, v4
	v_mov_b32_e32 v5, -1
	s_and_saveexec_b64 s[10:11], vcc
	s_cbranch_execz .LBB0_1391
	s_add_i32 s9, s61, 0x20840
	v_mov_b32_e32 v2, s9
	ds_read_b32 v2, v2
	s_waitcnt lgkmcnt(0)
	v_cmp_gt_i32_e32 vcc, v2, v4
	s_nop 1
	v_cndmask_b32_e64 v2, 16, 0, vcc
	v_or_b32_e32 v3, 8, v2
	v_lshl_add_u32 v5, v3, 2, s30
	ds_read_b32 v5, v5
	s_waitcnt lgkmcnt(0)
	v_cmp_gt_i32_e32 vcc, v5, v4
	s_nop 1
	v_cndmask_b32_e32 v2, v3, v2, vcc
	v_or_b32_e32 v3, 4, v2
	v_lshl_add_u32 v5, v3, 2, s30
	ds_read_b32 v5, v5
	s_waitcnt lgkmcnt(0)
	v_cmp_gt_i32_e32 vcc, v5, v4
	s_nop 1
	v_cndmask_b32_e32 v2, v3, v2, vcc
	v_or_b32_e32 v3, 2, v2
	v_lshl_add_u32 v5, v3, 2, s30
	ds_read_b32 v5, v5
	s_waitcnt lgkmcnt(0)
	v_cmp_gt_i32_e32 vcc, v5, v4
	s_nop 1
	v_cndmask_b32_e32 v2, v3, v2, vcc
	v_add_u32_e32 v3, 1, v2
	v_lshl_add_u32 v5, v3, 2, s30
	ds_read_b32 v5, v5
	s_waitcnt lgkmcnt(0)
	v_cmp_gt_i32_e32 vcc, v5, v4
	s_nop 1
	v_cndmask_b32_e32 v5, v3, v2, vcc
	v_lshl_add_u32 v6, v5, 2, s30
	ds_read2_b32 v[2:3], v6 offset1:33
	ds_read_b32 v6, v6 offset:264
	s_waitcnt lgkmcnt(1)
	v_sub_u32_e32 v4, v4, v2
	v_ashrrev_i32_e32 v2, 31, v4
	v_lshrrev_b32_e32 v2, 30, v2
	v_add_u32_e32 v7, v4, v2
	v_ashrrev_i32_e32 v2, 2, v7
	v_and_b32_e32 v7, -4, v7
	v_sub_u32_e32 v7, v4, v7

; __device__ __forceinline__ unsigned xb_ld(unsigned* p)              { unsigned GAS* g = (unsigned GAS*)p; asm volatile("" : "+s"(g)); return __hip_atomic_load(g, __ATOMIC_RELAXED, __HIP_MEMORY_SCOPE_AGENT); }
;     __device__ __forceinline__ int tile_of(int i) const { return (lo + rk + i * nw) / NTN; }
;     __device__ __forceinline__ void wait_tile(int i) const {
;         if (threadIdx.x == 0) { unsigned* w = done + tile_of(i); unsigned sp = 0u;
;             while (xb_ld(w) < 8u) { __builtin_amdgcn_s_sleep(1); if (++sp > (1u << 16)) break; } }
;     }
; template <class Epi, class Src>
; __device__ __forceinline__ void gemm_phase(LAS unsigned char* lds, const Src S, const Epi E) {
;     ...
;         if constexpr (Src::WAITS) { if (has_next) S.wait_tile(ui + 1); }
.LBB0_1410:
	s_xor_b64 s[16:17], s[28:29], -1
	s_and_b64 vcc, exec, s[16:17]
	s_mov_b64 s[18:19], s[2:3]
	s_cbranch_vccnz .LBB0_1417
	s_and_saveexec_b64 s[18:19], s[84:85]
	s_cbranch_execz .LBB0_1416
	s_mul_i32 s7, s64, s31
	s_add_i32 s7, s7, s60
	s_ashr_i32 s15, s7, 31
	s_lshr_b32 s15, s15, 30
	s_add_i32 s7, s7, s15
	s_ashr_i32 s20, s7, 2
	s_ashr_i32 s21, s20, 31
	s_lshl_b64 s[20:21], s[20:21], 2
	s_add_u32 s20, s36, s20
	s_addc_u32 s21, s37, s21
	s_mov_b32 s7, 0x10001
	v_cmp_lt_u32_e32 vcc, 7, v255
	s_cbranch_vccnz .Lg2_polled
	s_branch .LBB0_1414

; __device__ __forceinline__ unsigned xb_ld(unsigned* p)              { unsigned GAS* g = (unsigned GAS*)p; asm volatile("" : "+s"(g)); return __hip_atomic_load(g, __ATOMIC_RELAXED, __HIP_MEMORY_SCOPE_AGENT); }
;     __device__ __forceinline__ int tile_of(int i) const { return (lo + rk + i * nw) / NTN; }
;     __device__ __forceinline__ void wait_tile(int i) const {
;         if (threadIdx.x == 0) { unsigned* w = done + tile_of(i); unsigned sp = 0u;
;             while (xb_ld(w) < 8u) { __builtin_amdgcn_s_sleep(1); if (++sp > (1u << 16)) break; } }
.Lg2_polled:
	s_add_i32 s7, s64, 1
	s_mul_i32 s7, s7, s31
	s_add_i32 s7, s7, s60
	s_ashr_i32 s15, s7, 31
	s_lshr_b32 s15, s15, 30
	s_add_i32 s7, s7, s15
	s_ashr_i32 s20, s7, 2
	s_ashr_i32 s21, s20, 31
	s_lshl_b64 s[20:21], s[20:21], 2
	s_add_u32 s20, s36, s20
	s_addc_u32 s21, s37, s21
	global_load_dword v255, v35, s[20:21] sc1
